# P6 (output projection): workgroups start staggered in 4 groups (0/8/16/24us) so residual-read epilogue bursts interleave with other groups K-loops
# baseline (speedup 1.0000x reference)
; #define TB_LOAD(R_, t_) do { const int _t = (t_); if (_t < tot) { const int _b = _t / per, _r = _t % per; ttb_load(R_, src + (size_t)_b * K_ * N_, N_, (_r % kt) * 128, (_r / kt) * 64, C.tid); } } while (0)
; #define TB_STEP(R_, t_) do { const int _u = (t_); if (_u < tot) { LAS unsigned* tile = (LAS unsigned*)(C.lds + kbuf * 8192); ttb_put(R_, tile, C.tid); TB_LOAD(R_, _u + 4 * G); __syncthreads(); \
;         { const int _b = _u / per, _r = _u % per; ttb_finish(tile, dstb + (size_t)_b * K_ * (MAP_ == 2 ? 4096 : N_), K_, (_r % kt) * 128, (_r / kt) * 64, MAP_, C.tid); } kbuf ^= 1; } } while (0)
; __device__ __forceinline__ void ttb_load(TReg& R, const float* src, int ld, int k0, int n0, int tid) {
;     const int kr = tid >> 4, nq = tid & 15;
; #pragma unroll
;     for (int rep = 0; rep < 4; ++rep) R.v[rep] = __builtin_nontemporal_load((const f32x4*)(src + (size_t)(k0 + 4 * kr + rep) * ld + n0 + 4 * nq)); }
; template <int K_, int N_, int MAP_> __device__ __forceinline__ void tjob_b(const Ctx& C, int bid, int G, const float* src, unsigned char* dstb, int nbatch) {
;     constexpr int kt = K_ / 128, ntile = N_ / 64, per = kt * ntile; const int tot = per * nbatch;
;     TReg R0, R1, R2, R3; int kbuf = 0;
;     ...
;     TB_LOAD(R0, bid); TB_LOAD(R1, bid + G); TB_LOAD(R2, bid + 2 * G); TB_LOAD(R3, bid + 3 * G);
;     for (int t = bid; t < tot; t += 4 * G) { TB_STEP(R0, t); TB_STEP(R1, t + G); TB_STEP(R2, t + 2 * G); TB_STEP(R3, t + 3 * G); }
.LBB0_202:
	s_waitcnt vmcnt(0) lgkmcnt(0)
	v_mov_b64_e32 v[2:3], s[70:71]
	s_barrier
	flat_load_dwordx2 v[66:67], v[2:3] offset:200
	s_movk_i32 s8, 0x4000
	s_and_b64 s[6:7], s[2:3], exec
	s_cselect_b32 s25, s8, 0x2a00
	s_cmp_lt_i32 s1, s25
	s_cselect_b64 s[6:7], -1, 0
	s_cmp_ge_i32 s1, s25
	s_cbranch_scc1 .LBB0_204
	s_ashr_i32 s8, s1, 31
	s_lshr_b32 s8, s8, 23
	s_add_i32 s9, s1, s8
	s_ashr_i32 s8, s9, 9
	s_and_b32 s9, s9, 0xfe00
	s_sub_i32 s12, s1, s9
	s_sext_i32_i16 s13, s12
	s_bfe_u32 s13, s13, 0x4001b
	s_add_i32 s13, s12, s13
	s_sext_i32_i16 s26, s13
	s_and_b32 s13, s13, 0xfff0
	s_sub_i32 s12, s12, s13
	s_ashr_i32 s9, s8, 31
	s_sext_i32_i16 s27, s12
	s_lshl_b32 s12, s26, 2
	s_lshl_b64 s[8:9], s[8:9], 24
	s_andn2_b32 s12, s12, 63
	v_and_b32_e32 v4, -4, v69
	s_ashr_i32 s13, s12, 31
	s_waitcnt vmcnt(0) lgkmcnt(0)
	v_lshl_add_u64 v[2:3], v[66:67], 0, s[8:9]
	v_lshl_add_u32 v10, s27, 7, v4
	v_lshl_add_u64 v[2:3], s[12:13], 2, v[2:3]
	v_and_b32_e32 v4, 0xf0, v74
	v_mov_b32_e32 v5, 0
	v_ashrrev_i32_e32 v11, 31, v10
	v_lshl_add_u64 v[12:13], v[2:3], 0, v[4:5]
	v_lshlrev_b64 v[2:3], 13, v[10:11]
	v_lshl_add_u64 v[14:15], v[12:13], 0, v[2:3]
	v_or_b32_e32 v2, 1, v10
	v_ashrrev_i32_e32 v3, 31, v2
	v_lshlrev_b64 v[2:3], 13, v[2:3]
	v_lshl_add_u64 v[16:17], v[12:13], 0, v[2:3]
	flat_load_dwordx4 v[2:5], v[14:15] nt
	flat_load_dwordx4 v[6:9], v[16:17] nt
	v_or_b32_e32 v14, 2, v10
	v_ashrrev_i32_e32 v15, 31, v14
	v_or_b32_e32 v10, 3, v10
	v_lshlrev_b64 v[14:15], 13, v[14:15]
	v_ashrrev_i32_e32 v11, 31, v10
	v_lshl_add_u64 v[18:19], v[12:13], 0, v[14:15]
	v_lshlrev_b64 v[10:11], 13, v[10:11]
	v_lshl_add_u64 v[20:21], v[12:13], 0, v[10:11]
	flat_load_dwordx4 v[10:13], v[18:19] nt
	flat_load_dwordx4 v[14:17], v[20:21] nt

; #define TB_LOAD(R_, t_) do { const int _t = (t_); if (_t < tot) { const int _b = _t / per, _r = _t % per; ttb_load(R_, src + (size_t)_b * K_ * N_, N_, (_r % kt) * 128, (_r / kt) * 64, C.tid); } } while (0)
; #define TB_STEP(R_, t_) do { const int _u = (t_); if (_u < tot) { LAS unsigned* tile = (LAS unsigned*)(C.lds + kbuf * 8192); ttb_put(R_, tile, C.tid); TB_LOAD(R_, _u + 4 * G); __syncthreads(); \
;         { const int _b = _u / per, _r = _u % per; ttb_finish(tile, dstb + (size_t)_b * K_ * (MAP_ == 2 ? 4096 : N_), K_, (_r % kt) * 128, (_r / kt) * 64, MAP_, C.tid); } kbuf ^= 1; } } while (0)
; __device__ __forceinline__ void fresh_tid(Ctx& C) { int t = threadIdx.x; asm volatile("" : "+v"(t)); C.tid = t; C.lane = t & 63; const Args* k = C.ka; asm volatile("" : "+s"(k)); C.ka = k; }
; template <int K_, int N_, int MAP_> __device__ __forceinline__ void tjob_b(const Ctx& C, int bid, int G, const float* src, unsigned char* dstb, int nbatch) {
;     constexpr int kt = K_ / 128, ntile = N_ / 64, per = kt * ntile; const int tot = per * nbatch;
;     TReg R0, R1, R2, R3; int kbuf = 0;
;     ...
;     TB_LOAD(R0, bid); TB_LOAD(R1, bid + G); TB_LOAD(R2, bid + 2 * G); TB_LOAD(R3, bid + 3 * G);
;     for (int t = bid; t < tot; t += 4 * G) { TB_STEP(R0, t); TB_STEP(R1, t + G); TB_STEP(R2, t + 2 * G); TB_STEP(R3, t + 3 * G); }
; __global__ void __launch_bounds__(512, 2) mk_fwd(Args args) {
;     ...
;         fresh_tid(C); if (nconv) tjob_b<2048, 2048, 0>(C, C.bid, Gg, C.ka->in[I_WE2] + (size_t)(NEXP - E2_TAIL) * FF * D_, C.ws + WS_W2T + (size_t)(NEXP - E2_TAIL) * FF * D_, E2_TAIL);
.LBB0_269:
	v_mov_b32_e32 v70, v0
	s_andn2_b64 vcc, exec, s[20:21]
	s_mov_b64 s[0:1], s[70:71]
	s_cbranch_vccnz .LBB0_278
	v_mov_b64_e32 v[2:3], s[0:1]
	flat_load_dwordx2 v[2:3], v[2:3] offset:200
	v_readlane_b32 s10, v254, 0
	s_mov_b64 s[70:71], s[0:1]
	s_cmpk_lt_i32 s10, 0x1600
	s_mov_b64 s[0:1], 0x15000000
	v_ashrrev_i32_e32 v72, 2, v70
	s_cselect_b64 s[2:3], -1, 0
	s_cmpk_gt_i32 s10, 0x15ff
	v_lshlrev_b32_e32 v1, 4, v70
	v_readlane_b32 s11, v254, 1
	s_waitcnt vmcnt(0) lgkmcnt(0)
	v_lshl_add_u64 v[66:67], v[2:3], 0, s[0:1]
	s_cbranch_scc1 .LBB0_272
	s_ashr_i32 s0, s10, 31
	s_lshr_b32 s0, s0, 23
	s_add_i32 s1, s10, s0
	s_ashr_i32 s0, s1, 9
	s_and_b32 s1, s1, 0xfe00
	s_sub_i32 s6, s10, s1
	s_sext_i32_i16 s7, s6
	s_bfe_u32 s7, s7, 0x4001b
	s_add_i32 s7, s6, s7
	s_sext_i32_i16 s8, s7
	s_and_b32 s7, s7, 0xfff0
	s_sub_i32 s6, s6, s7
	s_ashr_i32 s1, s0, 31
	s_sext_i32_i16 s9, s6
	s_lshl_b32 s6, s8, 2
	s_lshl_b64 s[0:1], s[0:1], 24
	s_andn2_b32 s6, s6, 63
	v_and_b32_e32 v4, -4, v72
	s_ashr_i32 s7, s6, 31
	v_lshl_add_u64 v[2:3], v[66:67], 0, s[0:1]
	v_lshl_add_u32 v10, s9, 7, v4
	v_lshl_add_u64 v[2:3], s[6:7], 2, v[2:3]
	v_and_b32_e32 v4, 0xf0, v1
	v_mov_b32_e32 v5, 0
	v_ashrrev_i32_e32 v11, 31, v10
	v_lshl_add_u64 v[12:13], v[2:3], 0, v[4:5]
	v_lshlrev_b64 v[2:3], 13, v[10:11]
	v_lshl_add_u64 v[14:15], v[12:13], 0, v[2:3]
	v_or_b32_e32 v2, 1, v10
	v_ashrrev_i32_e32 v3, 31, v2
	v_lshlrev_b64 v[2:3], 13, v[2:3]
	v_lshl_add_u64 v[16:17], v[12:13], 0, v[2:3]
	flat_load_dwordx4 v[2:5], v[14:15] nt
	flat_load_dwordx4 v[6:9], v[16:17] nt
	v_or_b32_e32 v14, 2, v10
	v_ashrrev_i32_e32 v15, 31, v14
	v_or_b32_e32 v10, 3, v10
	v_lshlrev_b64 v[14:15], 13, v[14:15]
	v_ashrrev_i32_e32 v11, 31, v10
	v_lshl_add_u64 v[18:19], v[12:13], 0, v[14:15]
	v_lshlrev_b64 v[10:11], 13, v[10:11]
	v_lshl_add_u64 v[20:21], v[12:13], 0, v[10:11]
	flat_load_dwordx4 v[10:13], v[18:19] nt
	flat_load_dwordx4 v[14:17], v[20:21] nt
.LBB0_272:
	s_add_i32 s0, s28, s10
	s_cmpk_gt_i32 s0, 0x15ff
	s_cbranch_scc1 .LBB0_274
	s_ashr_i32 s1, s0, 31
	s_lshr_b32 s1, s1, 23
	s_add_i32 s1, s0, s1
	s_ashr_i32 s6, s1, 9
	s_and_b32 s1, s1, 0xfe00
	s_sub_i32 s1, s0, s1
	s_sext_i32_i16 s8, s1
	s_bfe_u32 s8, s8, 0x4001b
	s_add_i32 s8, s1, s8
	s_sext_i32_i16 s9, s8
	s_and_b32 s8, s8, 0xfff0
	s_ashr_i32 s7, s6, 31
	s_sub_i32 s1, s1, s8
	s_lshl_b32 s8, s9, 2
	s_lshl_b64 s[6:7], s[6:7], 24
	s_sext_i32_i16 s1, s1
	s_andn2_b32 s8, s8, 63
	v_and_b32_e32 v20, -4, v72
	s_ashr_i32 s9, s8, 31
	v_lshl_add_u64 v[18:19], v[66:67], 0, s[6:7]
	v_lshl_add_u32 v26, s1, 7, v20
	v_lshl_add_u64 v[18:19], s[8:9], 2, v[18:19]
	v_and_b32_e32 v20, 0xf0, v1
	v_mov_b32_e32 v21, 0
	v_ashrrev_i32_e32 v27, 31, v26
	v_lshl_add_u64 v[28:29], v[18:19], 0, v[20:21]
	v_lshlrev_b64 v[18:19], 13, v[26:27]
	v_lshl_add_u64 v[30:31], v[28:29], 0, v[18:19]
	v_or_b32_e32 v18, 1, v26
	v_ashrrev_i32_e32 v19, 31, v18
	v_lshlrev_b64 v[18:19], 13, v[18:19]
	v_lshl_add_u64 v[32:33], v[28:29], 0, v[18:19]
	flat_load_dwordx4 v[18:21], v[30:31] nt
	flat_load_dwordx4 v[22:25], v[32:33] nt
	v_or_b32_e32 v30, 2, v26
	v_ashrrev_i32_e32 v31, 31, v30
	v_or_b32_e32 v26, 3, v26
	v_lshlrev_b64 v[30:31], 13, v[30:31]
	v_ashrrev_i32_e32 v27, 31, v26
	v_lshl_add_u64 v[34:35], v[28:29], 0, v[30:31]
	v_lshlrev_b64 v[26:27], 13, v[26:27]
	v_lshl_add_u64 v[36:37], v[28:29], 0, v[26:27]
	flat_load_dwordx4 v[26:29], v[34:35] nt
	flat_load_dwordx4 v[30:33], v[36:37] nt
.LBB0_274:
	s_add_i32 s0, s0, s28
	s_cmpk_gt_i32 s0, 0x15ff
	s_cbranch_scc1 .LBB0_276
	s_ashr_i32 s1, s0, 31
	s_lshr_b32 s1, s1, 23
	s_add_i32 s1, s0, s1
	s_ashr_i32 s6, s1, 9
	s_and_b32 s1, s1, 0xfe00
	s_sub_i32 s1, s0, s1
	s_sext_i32_i16 s8, s1
	s_bfe_u32 s8, s8, 0x4001b
	s_add_i32 s8, s1, s8
	s_sext_i32_i16 s9, s8
	s_and_b32 s8, s8, 0xfff0
	s_ashr_i32 s7, s6, 31
	s_sub_i32 s1, s1, s8
	s_lshl_b32 s8, s9, 2
	s_lshl_b64 s[6:7], s[6:7], 24
	s_sext_i32_i16 s1, s1
	s_andn2_b32 s8, s8, 63
	v_and_b32_e32 v36, -4, v72
	s_ashr_i32 s9, s8, 31
	v_lshl_add_u64 v[34:35], v[66:67], 0, s[6:7]
	v_lshl_add_u32 v42, s1, 7, v36
	v_lshl_add_u64 v[34:35], s[8:9], 2, v[34:35]
	v_and_b32_e32 v36, 0xf0, v1
	v_mov_b32_e32 v37, 0
	v_ashrrev_i32_e32 v43, 31, v42
	v_lshl_add_u64 v[44:45], v[34:35], 0, v[36:37]
	v_lshlrev_b64 v[34:35], 13, v[42:43]
	v_lshl_add_u64 v[46:47], v[44:45], 0, v[34:35]
	v_or_b32_e32 v34, 1, v42
	v_ashrrev_i32_e32 v35, 31, v34
	v_lshlrev_b64 v[34:35], 13, v[34:35]
	v_lshl_add_u64 v[48:49], v[44:45], 0, v[34:35]
	flat_load_dwordx4 v[34:37], v[46:47] nt
	flat_load_dwordx4 v[38:41], v[48:49] nt
	v_or_b32_e32 v46, 2, v42
	v_ashrrev_i32_e32 v47, 31, v46
	v_or_b32_e32 v42, 3, v42
	v_lshlrev_b64 v[46:47], 13, v[46:47]
	v_ashrrev_i32_e32 v43, 31, v42
	v_lshl_add_u64 v[50:51], v[44:45], 0, v[46:47]
	v_lshlrev_b64 v[42:43], 13, v[42:43]
	v_lshl_add_u64 v[52:53], v[44:45], 0, v[42:43]
	flat_load_dwordx4 v[42:45], v[50:51] nt
	flat_load_dwordx4 v[46:49], v[52:53] nt
.LBB0_276:
	s_add_i32 s0, s0, s28
	s_cmpk_gt_i32 s0, 0x15ff
	s_cbranch_scc1 .LBB0_279
	s_ashr_i32 s1, s0, 31
	s_lshr_b32 s1, s1, 23
	s_add_i32 s1, s0, s1
	s_ashr_i32 s6, s1, 9
	s_and_b32 s1, s1, 0xfe00
	s_sub_i32 s8, s0, s1
	s_ashr_i32 s7, s6, 31
	s_lshl_b64 s[0:1], s[6:7], 24
	s_sext_i32_i16 s6, s8
	s_bfe_u32 s6, s6, 0x4001b
	s_add_i32 s6, s8, s6
	s_sext_i32_i16 s7, s6
	s_and_b32 s6, s6, 0xfff0
	s_sub_i32 s6, s8, s6
	s_sext_i32_i16 s8, s6
	s_lshl_b32 s6, s7, 2
	s_andn2_b32 s6, s6, 63
	v_and_b32_e32 v52, -4, v72
	s_ashr_i32 s7, s6, 31
	v_lshl_add_u64 v[50:51], v[66:67], 0, s[0:1]
	v_lshl_add_u32 v58, s8, 7, v52
	v_lshl_add_u64 v[50:51], s[6:7], 2, v[50:51]
	v_and_b32_e32 v52, 0xf0, v1
	v_mov_b32_e32 v53, 0
	v_ashrrev_i32_e32 v59, 31, v58
	v_lshl_add_u64 v[60:61], v[50:51], 0, v[52:53]
	v_lshlrev_b64 v[50:51], 13, v[58:59]
	v_lshl_add_u64 v[62:63], v[60:61], 0, v[50:51]
	v_or_b32_e32 v50, 1, v58
	v_ashrrev_i32_e32 v51, 31, v50
	v_lshlrev_b64 v[50:51], 13, v[50:51]
	v_lshl_add_u64 v[64:65], v[60:61], 0, v[50:51]
	flat_load_dwordx4 v[50:53], v[62:63] nt
	flat_load_dwordx4 v[54:57], v[64:65] nt
	v_or_b32_e32 v62, 2, v58
	v_ashrrev_i32_e32 v63, 31, v62
	v_or_b32_e32 v58, 3, v58
	v_lshlrev_b64 v[62:63], 13, v[62:63]
	v_ashrrev_i32_e32 v59, 31, v58
	v_lshl_add_u64 v[68:69], v[60:61], 0, v[62:63]
	v_lshlrev_b64 v[58:59], 13, v[58:59]
	v_lshl_add_u64 v[74:75], v[60:61], 0, v[58:59]
	flat_load_dwordx4 v[58:61], v[68:69] nt
	flat_load_dwordx4 v[62:65], v[74:75] nt
	s_andn2_b64 vcc, exec, s[2:3]
	s_cbranch_vccnz .LBB0_296
	s_branch .LBB0_280

; #define LAS __attribute__((address_space(3)))
; #define TB_LOAD(R_, t_) do { const int _t = (t_); if (_t < tot) { const int _b = _t / per, _r = _t % per; ttb_load(R_, src + (size_t)_b * K_ * N_, N_, (_r % kt) * 128, (_r / kt) * 64, C.tid); } } while (0)
; #define TB_STEP(R_, t_) do { const int _u = (t_); if (_u < tot) { LAS unsigned* tile = (LAS unsigned*)(C.lds + kbuf * 8192); ttb_put(R_, tile, C.tid); TB_LOAD(R_, _u + 4 * G); __syncthreads(); \
;         { const int _b = _u / per, _r = _u % per; ttb_finish(tile, dstb + (size_t)_b * K_ * (MAP_ == 2 ? 4096 : N_), K_, (_r % kt) * 128, (_r / kt) * 64, MAP_, C.tid); } kbuf ^= 1; } } while (0)
; __device__ __forceinline__ void ttb_put(const TReg& R, LAS unsigned* tile, int tid) {
;     const int kr = tid >> 4, nq = tid & 15;
; #pragma unroll
;     for (int c = 0; c < 4; ++c) { const int n = 4 * nq + c;
;         tile[n * 32 + (kr ^ (n & 31))] = pk4_fp8(R.v[0][c] * W_FP8_SCALE, R.v[1][c] * W_FP8_SCALE, R.v[2][c] * W_FP8_SCALE, R.v[3][c] * W_FP8_SCALE); } }
; __device__ __forceinline__ void ttb_finish(LAS const unsigned* tile, unsigned char* dst, int ldd, int k0, int n0, int map, int tid) {
;     const int n = tid >> 3, kq = tid & 7, m = n & 31, ns = n0 + n; int r = ns;
;     if (map == 2) { const int j = ns >> 1, par = ns & 1; r = 256 * (j >> 7) + 128 * par + (j & 127); }
;     const u32x4 g = *(LAS const u32x4*)(tile + n * 32 + 4 * (kq ^ (m >> 2)));
;     const unsigned a0 = (m & 1) ? g.y : g.x, a1 = (m & 1) ? g.x : g.y, a2 = (m & 1) ? g.w : g.z, a3 = (m & 1) ? g.z : g.w;
;     u32x4 w; w.x = (m & 2) ? a2 : a0; w.y = (m & 2) ? a3 : a1; w.z = (m & 2) ? a0 : a2; w.w = (m & 2) ? a1 : a3;
;     __builtin_nontemporal_store(w, (u32x4*)(dst + (size_t)r * ldd + k0 + 16 * kq));
; }
; template <int K_, int N_, int MAP_> __device__ __forceinline__ void tjob_b(const Ctx& C, int bid, int G, const float* src, unsigned char* dstb, int nbatch) {
;     constexpr int kt = K_ / 128, ntile = N_ / 64, per = kt * ntile; const int tot = per * nbatch;
;     TReg R0, R1, R2, R3; int kbuf = 0;
;     ...
;     TB_LOAD(R0, bid); TB_LOAD(R1, bid + G); TB_LOAD(R2, bid + 2 * G); TB_LOAD(R3, bid + 3 * G);
;     for (int t = bid; t < tot; t += 4 * G) { TB_STEP(R0, t); TB_STEP(R1, t + G); TB_STEP(R2, t + 2 * G); TB_STEP(R3, t + 3 * G); }
.LBB0_280:
	v_lshlrev_b32_e32 v1, 2, v70
	v_and_b32_e32 v68, 60, v1
	v_ashrrev_i32_e32 v71, 4, v70
	v_or_b32_e32 v73, 2, v68
	v_readlane_b32 s2, v254, 2
	v_or_b32_e32 v69, 1, v68
	v_bitop3_b32 v82, v73, v71, 30 bitop3:0x6c
	v_lshlrev_b32_e32 v74, 7, v73
	v_or_b32_e32 v73, 3, v68
	v_readlane_b32 s3, v254, 3
	s_add_u32 s0, s62, 0x2ed10000
	v_bitop3_b32 v80, v1, v71, 28 bitop3:0x6c
	v_bitop3_b32 v81, v69, v71, 29 bitop3:0x6c
	v_bitop3_b32 v83, v73, v71, 31 bitop3:0x6c
	v_and_b32_e32 v71, 7, v70
	s_mov_b32 s16, s2
	s_mul_i32 s2, s2, 7
	s_mul_i32 s3, s30, 7
	s_addc_u32 s1, s63, 0
	v_lshlrev_b32_e32 v75, 7, v73
	v_ashrrev_i32_e32 v76, 3, v70
	v_lshlrev_b32_e32 v73, 2, v71
	s_sub_i32 s14, s2, s3
	s_mul_i32 s2, s30, 6
	v_bitop3_b32 v84, v76, v73, 28 bitop3:0x6c
	v_and_b32_e32 v73, 8, v70
	s_sub_i32 s15, s29, s2
	s_mul_i32 s2, s16, 5
	s_mul_i32 s30, s30, 5
	v_cmp_eq_u32_e64 s[6:7], 0, v73
	v_and_b32_e32 v70, 16, v70
	v_mov_b32_e32 v73, 0
	s_sub_i32 s16, s2, s30
	v_readlane_b32 s2, v254, 0
	s_lshl_b32 s10, s28, 1
	s_mul_i32 s11, s28, 3
	s_lshl_b32 s12, s28, 2
	v_lshlrev_b32_e32 v1, 7, v68
	v_lshlrev_b32_e32 v69, 7, v69
	v_lshlrev_b32_e32 v77, 7, v76
	s_mov_b32 s13, 0
	v_cmp_eq_u32_e64 s[8:9], 0, v70
	v_lshlrev_b32_e32 v70, 4, v71
	v_mov_b32_e32 v71, v73
	v_and_b32_e32 v78, -4, v72
	s_mov_b32 s17, 0xc3e00000
	v_mov_b32_e32 v79, 0x43e00000
	v_lshlrev_b32_e32 v80, 2, v80
	v_lshlrev_b32_e32 v81, 2, v81
	v_lshlrev_b32_e32 v82, 2, v82
	v_lshlrev_b32_e32 v83, 2, v83
	v_lshlrev_b32_e32 v84, 2, v84
	s_mov_b32 s19, s2
	v_readlane_b32 s3, v254, 1
	s_branch .LBB0_283

; #define LAS __attribute__((address_space(3)))
; #define TB_LOAD(R_, t_) do { const int _t = (t_); if (_t < tot) { const int _b = _t / per, _r = _t % per; ttb_load(R_, src + (size_t)_b * K_ * N_, N_, (_r % kt) * 128, (_r / kt) * 64, C.tid); } } while (0)
; __device__ __forceinline__ void ttb_load(TReg& R, const float* src, int ld, int k0, int n0, int tid) {
;     const int kr = tid >> 4, nq = tid & 15;
; #pragma unroll
;     for (int rep = 0; rep < 4; ++rep) R.v[rep] = __builtin_nontemporal_load((const f32x4*)(src + (size_t)(k0 + 4 * kr + rep) * ld + n0 + 4 * nq)); }
; __device__ __forceinline__ void ttb_put(const TReg& R, LAS unsigned* tile, int tid) {
;     const int kr = tid >> 4, nq = tid & 15;
; #pragma unroll
;     for (int c = 0; c < 4; ++c) { const int n = 4 * nq + c;
;         tile[n * 32 + (kr ^ (n & 31))] = pk4_fp8(R.v[0][c] * W_FP8_SCALE, R.v[1][c] * W_FP8_SCALE, R.v[2][c] * W_FP8_SCALE, R.v[3][c] * W_FP8_SCALE); } }
; __device__ __forceinline__ void ttb_finish(LAS const unsigned* tile, unsigned char* dst, int ldd, int k0, int n0, int map, int tid) {
;     const int n = tid >> 3, kq = tid & 7, m = n & 31, ns = n0 + n; int r = ns;
;     if (map == 2) { const int j = ns >> 1, par = ns & 1; r = 256 * (j >> 7) + 128 * par + (j & 127); }
;     const u32x4 g = *(LAS const u32x4*)(tile + n * 32 + 4 * (kq ^ (m >> 2)));
;     const unsigned a0 = (m & 1) ? g.y : g.x, a1 = (m & 1) ? g.x : g.y, a2 = (m & 1) ? g.w : g.z, a3 = (m & 1) ? g.z : g.w;
;     u32x4 w; w.x = (m & 2) ? a2 : a0; w.y = (m & 2) ? a3 : a1; w.z = (m & 2) ? a0 : a2; w.w = (m & 2) ? a1 : a3;
;     __builtin_nontemporal_store(w, (u32x4*)(dst + (size_t)r * ldd + k0 + 16 * kq));
; }
; template <int K_, int N_, int MAP_> __device__ __forceinline__ void tjob_b(const Ctx& C, int bid, int G, const float* src, unsigned char* dstb, int nbatch) {
;     constexpr int kt = K_ / 128, ntile = N_ / 64, per = kt * ntile; const int tot = per * nbatch;
;     TReg R0, R1, R2, R3; int kbuf = 0;
;     ...
;     TB_LOAD(R0, bid); TB_LOAD(R1, bid + G); TB_LOAD(R2, bid + 2 * G); TB_LOAD(R3, bid + 3 * G);
;     for (int t = bid; t < tot; t += 4 * G) { TB_STEP(R0, t); TB_STEP(R1, t + G); TB_STEP(R2, t + 2 * G); TB_STEP(R3, t + 3 * G); }
.LBB0_283:
	s_waitcnt vmcnt(0) lgkmcnt(0)
	v_mul_f32_e32 v72, 0x43800000, v2
	v_mul_f32_e32 v85, 0x43800000, v6
	v_med3_f32 v72, v72, s17, v79
	v_med3_f32 v85, v85, s17, v79
	v_mov_b32_e32 v87, 0
	v_cvt_pk_fp8_f32 v87, v72, v85
	v_mul_f32_e32 v86, 0x43800000, v10
	v_mul_f32_e32 v72, 0x43800000, v14
	v_med3_f32 v85, v86, s17, v79
	v_med3_f32 v72, v72, s17, v79
	v_cvt_pk_fp8_f32 v87, v85, v72 op_sel:[0,0,1]
	v_mul_f32_e32 v72, 0x43800000, v3
	v_mul_f32_e32 v85, 0x43800000, v7
	v_med3_f32 v72, v72, s17, v79
	v_med3_f32 v85, v85, s17, v79
	v_mov_b32_e32 v88, 0
	v_cvt_pk_fp8_f32 v88, v72, v85
	v_mul_f32_e32 v86, 0x43800000, v11
	v_mul_f32_e32 v72, 0x43800000, v15
	v_med3_f32 v85, v86, s17, v79
	v_med3_f32 v72, v72, s17, v79
	s_lshl_b32 s2, s13, 13
	v_cvt_pk_fp8_f32 v88, v85, v72 op_sel:[0,0,1]
	s_add_i32 s20, s2, 0
	v_add3_u32 v72, s20, v1, v80
	ds_write_b32 v72, v87
	v_add3_u32 v72, s20, v69, v81
	ds_write_b32 v72, v88
	v_mul_f32_e32 v72, 0x43800000, v4
	v_mul_f32_e32 v85, 0x43800000, v8
	v_med3_f32 v72, v72, s17, v79
	v_med3_f32 v85, v85, s17, v79
	v_mov_b32_e32 v87, 0
	v_cvt_pk_fp8_f32 v87, v72, v85
	v_mul_f32_e32 v86, 0x43800000, v12
	v_mul_f32_e32 v72, 0x43800000, v16
	v_med3_f32 v85, v86, s17, v79
	v_med3_f32 v72, v72, s17, v79
	v_cvt_pk_fp8_f32 v87, v85, v72 op_sel:[0,0,1]
	v_mul_f32_e32 v72, 0x43800000, v5
	v_mul_f32_e32 v85, 0x43800000, v9
	v_med3_f32 v72, v72, s17, v79
	v_med3_f32 v85, v85, s17, v79
	v_mov_b32_e32 v88, 0
	v_cvt_pk_fp8_f32 v88, v72, v85
	v_mul_f32_e32 v86, 0x43800000, v13
	v_mul_f32_e32 v72, 0x43800000, v17
	v_med3_f32 v85, v86, s17, v79
	v_med3_f32 v72, v72, s17, v79
	v_cvt_pk_fp8_f32 v88, v85, v72 op_sel:[0,0,1]
	s_add_i32 s18, s19, s12
	s_cmpk_gt_i32 s18, 0x15ff
	v_add3_u32 v72, s20, v74, v82
	s_cselect_b64 s[2:3], -1, 0
	ds_write_b32 v72, v87
	v_add3_u32 v72, s20, v75, v83
	s_and_b64 vcc, exec, s[2:3]
	ds_write_b32 v72, v88
	s_cbranch_vccnz .LBB0_285
	s_ashr_i32 s21, s18, 31
	s_lshr_b32 s21, s21, 23
	s_add_i32 s21, s18, s21
	s_ashr_i32 s22, s21, 9
	s_and_b32 s21, s21, 0xfe00
	s_ashr_i32 s23, s22, 31
	s_sub_i32 s21, s18, s21
	s_lshl_b64 s[22:23], s[22:23], 24
	v_lshl_add_u64 v[2:3], v[66:67], 0, s[22:23]
	s_sext_i32_i16 s22, s21
	s_bfe_u32 s22, s22, 0x4001b
	s_add_i32 s22, s21, s22
	s_sext_i32_i16 s23, s22
	s_and_b32 s22, s22, 0xfff0
	s_sub_i32 s21, s21, s22
	s_lshl_b32 s22, s23, 2
	s_sext_i32_i16 s21, s21
	s_andn2_b32 s22, s22, 63
	v_lshl_add_u32 v10, s21, 7, v78
	s_ashr_i32 s23, s22, 31
	v_lshl_add_u64 v[2:3], s[22:23], 2, v[2:3]
	v_lshlrev_b32_e32 v72, 2, v68
	v_ashrrev_i32_e32 v11, 31, v10
	v_lshl_add_u64 v[12:13], v[2:3], 0, v[72:73]
	v_lshlrev_b64 v[2:3], 13, v[10:11]
	v_lshl_add_u64 v[14:15], v[12:13], 0, v[2:3]
	v_or_b32_e32 v2, 1, v10
	v_ashrrev_i32_e32 v3, 31, v2
	v_lshlrev_b64 v[2:3], 13, v[2:3]
	v_lshl_add_u64 v[16:17], v[12:13], 0, v[2:3]
	flat_load_dwordx4 v[2:5], v[14:15] nt
	flat_load_dwordx4 v[6:9], v[16:17] nt
	v_or_b32_e32 v14, 2, v10
	v_ashrrev_i32_e32 v15, 31, v14
	v_or_b32_e32 v10, 3, v10
	v_lshlrev_b64 v[14:15], 13, v[14:15]
	v_ashrrev_i32_e32 v11, 31, v10
	v_lshl_add_u64 v[86:87], v[12:13], 0, v[14:15]
	v_lshlrev_b64 v[10:11], 13, v[10:11]
	v_lshl_add_u64 v[88:89], v[12:13], 0, v[10:11]
	flat_load_dwordx4 v[10:13], v[86:87] nt
	flat_load_dwordx4 v[14:17], v[88:89] nt
.LBB0_285:
	s_ashr_i32 s21, s19, 31
	s_lshr_b32 s21, s21, 23
	s_add_i32 s21, s19, s21
	s_ashr_i32 s22, s21, 9
	s_and_b32 s21, s21, 0xfe00
	s_ashr_i32 s23, s22, 31
	s_sub_i32 s21, s19, s21
	s_lshl_b64 s[22:23], s[22:23], 22
	s_add_u32 s22, s0, s22
	s_sext_i32_i16 s24, s21
	s_addc_u32 s23, s1, s23
	s_bfe_u32 s24, s24, 0x4001b
	s_add_i32 s24, s21, s24
	v_add3_u32 v72, s20, v77, v84
	s_waitcnt lgkmcnt(0)
	s_barrier
	s_sext_i32_i16 s25, s24
	s_and_b32 s24, s24, 0xfff0
	ds_read_b128 v[86:89], v72
	s_sub_i32 s21, s21, s24
	s_sext_i32_i16 s21, s21
	s_lshl_b32 s20, s21, 7
	s_lshl_b32 s21, s25, 2
	s_andn2_b32 s21, s21, 63
	v_add_u32_e32 v90, s21, v76
	s_waitcnt lgkmcnt(0)
	v_cndmask_b32_e64 v72, v87, v86, s[6:7]
	v_cndmask_b32_e64 v91, v89, v88, s[6:7]
	v_cndmask_b32_e64 v85, v86, v87, s[6:7]
	v_cndmask_b32_e64 v89, v88, v89, s[6:7]
	v_cndmask_b32_e64 v86, v91, v72, s[8:9]
	v_cndmask_b32_e64 v88, v72, v91, s[8:9]
	v_ashrrev_i32_e32 v91, 31, v90
	v_lshlrev_b64 v[90:91], 11, v[90:91]
	v_lshl_add_u64 v[90:91], s[22:23], 0, v[90:91]
	s_ashr_i32 s21, s20, 31
	v_lshl_add_u64 v[90:91], v[90:91], 0, s[20:21]
	s_xor_b32 s21, s13, 1
	s_add_i32 s20, s28, s19
	v_cndmask_b32_e64 v87, v89, v85, s[8:9]
	v_cndmask_b32_e64 v89, v85, v89, s[8:9]
	v_lshl_add_u64 v[90:91], v[90:91], 0, v[70:71]
	s_cmpk_gt_i32 s20, 0x15ff
	global_store_dwordx4 v[90:91], v[86:89], off nt
	s_cbranch_scc1 .LBB0_289
	v_mul_f32_e32 v72, 0x43800000, v18
	v_mul_f32_e32 v85, 0x43800000, v22
	v_med3_f32 v72, v72, s17, v79
	v_med3_f32 v85, v85, s17, v79
	v_mov_b32_e32 v87, 0
	v_cvt_pk_fp8_f32 v87, v72, v85
	v_mul_f32_e32 v86, 0x43800000, v26
	v_mul_f32_e32 v72, 0x43800000, v30
	v_med3_f32 v85, v86, s17, v79
	v_med3_f32 v72, v72, s17, v79
	v_cvt_pk_fp8_f32 v87, v85, v72 op_sel:[0,0,1]
	s_lshl_b32 s21, s21, 13
	s_add_i32 s21, s21, 0
	v_add3_u32 v72, s21, v1, v80
	ds_write_b32 v72, v87
	v_mul_f32_e32 v72, 0x43800000, v19
	v_mul_f32_e32 v85, 0x43800000, v23
	v_med3_f32 v72, v72, s17, v79
	v_med3_f32 v85, v85, s17, v79
	v_mov_b32_e32 v87, 0
	v_cvt_pk_fp8_f32 v87, v72, v85
	v_mul_f32_e32 v86, 0x43800000, v27
	v_mul_f32_e32 v72, 0x43800000, v31
	v_med3_f32 v85, v86, s17, v79
	v_med3_f32 v72, v72, s17, v79
	v_cvt_pk_fp8_f32 v87, v85, v72 op_sel:[0,0,1]
	v_mul_f32_e32 v72, 0x43800000, v20
	v_mul_f32_e32 v85, 0x43800000, v24
	v_med3_f32 v72, v72, s17, v79
	v_med3_f32 v85, v85, s17, v79
	v_mov_b32_e32 v88, 0
	v_cvt_pk_fp8_f32 v88, v72, v85
	v_mul_f32_e32 v86, 0x43800000, v28
	v_mul_f32_e32 v72, 0x43800000, v32
	v_med3_f32 v85, v86, s17, v79
	v_med3_f32 v72, v72, s17, v79
	v_cvt_pk_fp8_f32 v88, v85, v72 op_sel:[0,0,1]
	v_add3_u32 v72, s21, v69, v81
	ds_write_b32 v72, v87
	v_add3_u32 v72, s21, v74, v82
	ds_write_b32 v72, v88
	v_mul_f32_e32 v72, 0x43800000, v21
	v_mul_f32_e32 v85, 0x43800000, v25
	v_med3_f32 v72, v72, s17, v79
	v_med3_f32 v85, v85, s17, v79
	v_mov_b32_e32 v87, 0
	v_cvt_pk_fp8_f32 v87, v72, v85
	v_mul_f32_e32 v86, 0x43800000, v29
	v_mul_f32_e32 v72, 0x43800000, v33
	v_med3_f32 v85, v86, s17, v79
	v_med3_f32 v72, v72, s17, v79
	v_cvt_pk_fp8_f32 v87, v85, v72 op_sel:[0,0,1]
	s_add_i32 s22, s16, s19
	v_add3_u32 v72, s21, v75, v83
	s_cmpk_gt_i32 s22, 0x15ff
	ds_write_b32 v72, v87
	s_cbranch_scc1 .LBB0_288
; #define LAS __attribute__((address_space(3)))
; #define TB_LOAD(R_, t_) do { const int _t = (t_); if (_t < tot) { const int _b = _t / per, _r = _t % per; ttb_load(R_, src + (size_t)_b * K_ * N_, N_, (_r % kt) * 128, (_r / kt) * 64, C.tid); } } while (0)
; __device__ __forceinline__ void ttb_load(TReg& R, const float* src, int ld, int k0, int n0, int tid) {
;     const int kr = tid >> 4, nq = tid & 15;
; #pragma unroll
;     for (int rep = 0; rep < 4; ++rep) R.v[rep] = __builtin_nontemporal_load((const f32x4*)(src + (size_t)(k0 + 4 * kr + rep) * ld + n0 + 4 * nq)); }
; __device__ __forceinline__ void ttb_put(const TReg& R, LAS unsigned* tile, int tid) {
;     const int kr = tid >> 4, nq = tid & 15;
; #pragma unroll
;     for (int c = 0; c < 4; ++c) { const int n = 4 * nq + c;
;         tile[n * 32 + (kr ^ (n & 31))] = pk4_fp8(R.v[0][c] * W_FP8_SCALE, R.v[1][c] * W_FP8_SCALE, R.v[2][c] * W_FP8_SCALE, R.v[3][c] * W_FP8_SCALE); } }
; __device__ __forceinline__ void ttb_finish(LAS const unsigned* tile, unsigned char* dst, int ldd, int k0, int n0, int map, int tid) {
;     const int n = tid >> 3, kq = tid & 7, m = n & 31, ns = n0 + n; int r = ns;
;     if (map == 2) { const int j = ns >> 1, par = ns & 1; r = 256 * (j >> 7) + 128 * par + (j & 127); }
;     const u32x4 g = *(LAS const u32x4*)(tile + n * 32 + 4 * (kq ^ (m >> 2)));
;     const unsigned a0 = (m & 1) ? g.y : g.x, a1 = (m & 1) ? g.x : g.y, a2 = (m & 1) ? g.w : g.z, a3 = (m & 1) ? g.z : g.w;
;     u32x4 w; w.x = (m & 2) ? a2 : a0; w.y = (m & 2) ? a3 : a1; w.z = (m & 2) ? a0 : a2; w.w = (m & 2) ? a1 : a3;
;     __builtin_nontemporal_store(w, (u32x4*)(dst + (size_t)r * ldd + k0 + 16 * kq));
; }
; template <int K_, int N_, int MAP_> __device__ __forceinline__ void tjob_b(const Ctx& C, int bid, int G, const float* src, unsigned char* dstb, int nbatch) {
;     constexpr int kt = K_ / 128, ntile = N_ / 64, per = kt * ntile; const int tot = per * nbatch;
;     TReg R0, R1, R2, R3; int kbuf = 0;
;     ...
;     TB_LOAD(R0, bid); TB_LOAD(R1, bid + G); TB_LOAD(R2, bid + 2 * G); TB_LOAD(R3, bid + 3 * G);
;     for (int t = bid; t < tot; t += 4 * G) { TB_STEP(R0, t); TB_STEP(R1, t + G); TB_STEP(R2, t + 2 * G); TB_STEP(R3, t + 3 * G); }
	s_ashr_i32 s23, s22, 31
	s_lshr_b32 s23, s23, 23
	s_add_i32 s23, s22, s23
	s_ashr_i32 s24, s23, 9
	s_and_b32 s23, s23, 0xfe00
	s_ashr_i32 s25, s24, 31
	s_sub_i32 s26, s22, s23
	s_lshl_b64 s[22:23], s[24:25], 24
	v_lshl_add_u64 v[18:19], v[66:67], 0, s[22:23]
	s_sext_i32_i16 s22, s26
	s_bfe_u32 s22, s22, 0x4001b
	s_add_i32 s22, s26, s22
	s_sext_i32_i16 s23, s22
	s_and_b32 s22, s22, 0xfff0
	s_sub_i32 s22, s26, s22
	s_sext_i32_i16 s24, s22
	s_lshl_b32 s22, s23, 2
	s_andn2_b32 s22, s22, 63
	v_lshl_add_u32 v26, s24, 7, v78
	s_ashr_i32 s23, s22, 31
	v_lshl_add_u64 v[18:19], s[22:23], 2, v[18:19]
	v_lshlrev_b32_e32 v72, 2, v68
	v_ashrrev_i32_e32 v27, 31, v26
	v_lshl_add_u64 v[28:29], v[18:19], 0, v[72:73]
	v_lshlrev_b64 v[18:19], 13, v[26:27]
	v_lshl_add_u64 v[30:31], v[28:29], 0, v[18:19]
	v_or_b32_e32 v18, 1, v26
	v_ashrrev_i32_e32 v19, 31, v18
	v_lshlrev_b64 v[18:19], 13, v[18:19]
	v_lshl_add_u64 v[32:33], v[28:29], 0, v[18:19]
	flat_load_dwordx4 v[18:21], v[30:31] nt
	flat_load_dwordx4 v[22:25], v[32:33] nt
	v_or_b32_e32 v30, 2, v26
	v_ashrrev_i32_e32 v31, 31, v30
	v_or_b32_e32 v26, 3, v26
	v_lshlrev_b64 v[30:31], 13, v[30:31]
	v_ashrrev_i32_e32 v27, 31, v26
	v_lshl_add_u64 v[86:87], v[28:29], 0, v[30:31]
	v_lshlrev_b64 v[26:27], 13, v[26:27]
	v_lshl_add_u64 v[88:89], v[28:29], 0, v[26:27]
	flat_load_dwordx4 v[26:29], v[86:87] nt
	flat_load_dwordx4 v[30:33], v[88:89] nt
.LBB0_288:
	s_ashr_i32 s22, s20, 31
	s_lshr_b32 s22, s22, 23
	s_add_i32 s23, s20, s22
	s_ashr_i32 s22, s23, 9
	s_and_b32 s23, s23, 0xfe00
	s_sub_i32 s20, s20, s23
	s_ashr_i32 s23, s22, 31
	s_lshl_b64 s[22:23], s[22:23], 22
	s_add_u32 s22, s0, s22
	s_sext_i32_i16 s24, s20
	v_add3_u32 v72, s21, v77, v84
	s_waitcnt lgkmcnt(0)
	s_barrier
	s_addc_u32 s23, s1, s23
	s_bfe_u32 s24, s24, 0x4001b
	ds_read_b128 v[86:89], v72
	s_add_i32 s24, s20, s24
	s_sext_i32_i16 s25, s24
	s_lshl_b32 s21, s25, 2
	s_and_b32 s24, s24, 0xfff0
	s_andn2_b32 s21, s21, 63
	s_sub_i32 s20, s20, s24
	v_add_u32_e32 v90, s21, v76
	s_waitcnt lgkmcnt(0)
	v_cndmask_b32_e64 v72, v87, v86, s[6:7]
	v_cndmask_b32_e64 v91, v89, v88, s[6:7]
	s_sext_i32_i16 s20, s20
	v_cndmask_b32_e64 v85, v86, v87, s[6:7]
	v_cndmask_b32_e64 v89, v88, v89, s[6:7]
	v_cndmask_b32_e64 v86, v91, v72, s[8:9]
	v_cndmask_b32_e64 v88, v72, v91, s[8:9]
	v_ashrrev_i32_e32 v91, 31, v90
	s_lshl_b32 s20, s20, 7
	v_lshlrev_b64 v[90:91], 11, v[90:91]
	v_lshl_add_u64 v[90:91], s[22:23], 0, v[90:91]
	s_ashr_i32 s21, s20, 31
	v_lshl_add_u64 v[90:91], v[90:91], 0, s[20:21]
	v_cndmask_b32_e64 v87, v89, v85, s[8:9]
	v_cndmask_b32_e64 v89, v85, v89, s[8:9]
	v_lshl_add_u64 v[90:91], v[90:91], 0, v[70:71]
	global_store_dwordx4 v[90:91], v[86:89], off nt
	s_add_i32 s20, s10, s19
	s_cmpk_gt_i32 s20, 0x15ff
	s_cbranch_scc0 .LBB0_290
	s_branch .LBB0_293
.LBB0_289:
	s_mov_b32 s13, s21
	s_add_i32 s20, s10, s19
	s_cmpk_gt_i32 s20, 0x15ff
	s_cbranch_scc1 .LBB0_293
.LBB0_290:
	v_mul_f32_e32 v72, 0x43800000, v34
	v_mul_f32_e32 v85, 0x43800000, v38
	v_med3_f32 v72, v72, s17, v79
	v_med3_f32 v85, v85, s17, v79
	v_mov_b32_e32 v87, 0
	v_cvt_pk_fp8_f32 v87, v72, v85
	v_mul_f32_e32 v86, 0x43800000, v42
	v_mul_f32_e32 v72, 0x43800000, v46
	v_med3_f32 v85, v86, s17, v79
	v_med3_f32 v72, v72, s17, v79
	v_cvt_pk_fp8_f32 v87, v85, v72 op_sel:[0,0,1]
	s_lshl_b32 s21, s13, 13
	s_add_i32 s21, s21, 0
	v_add3_u32 v72, s21, v1, v80
	ds_write_b32 v72, v87
	v_mul_f32_e32 v72, 0x43800000, v35
	v_mul_f32_e32 v85, 0x43800000, v39
	v_med3_f32 v72, v72, s17, v79
	v_med3_f32 v85, v85, s17, v79
	v_mov_b32_e32 v87, 0
	v_cvt_pk_fp8_f32 v87, v72, v85
	v_mul_f32_e32 v86, 0x43800000, v43
	v_mul_f32_e32 v72, 0x43800000, v47
	v_med3_f32 v85, v86, s17, v79
	v_med3_f32 v72, v72, s17, v79
	v_cvt_pk_fp8_f32 v87, v85, v72 op_sel:[0,0,1]
	v_mul_f32_e32 v72, 0x43800000, v36
	v_mul_f32_e32 v85, 0x43800000, v40
	v_med3_f32 v72, v72, s17, v79
	v_med3_f32 v85, v85, s17, v79
	v_mov_b32_e32 v88, 0
	v_cvt_pk_fp8_f32 v88, v72, v85
	v_mul_f32_e32 v86, 0x43800000, v44
	v_mul_f32_e32 v72, 0x43800000, v48
	v_med3_f32 v85, v86, s17, v79
	v_med3_f32 v72, v72, s17, v79
	v_cvt_pk_fp8_f32 v88, v85, v72 op_sel:[0,0,1]
	v_add3_u32 v72, s21, v69, v81
	ds_write_b32 v72, v87
	v_add3_u32 v72, s21, v74, v82
	ds_write_b32 v72, v88
	v_mul_f32_e32 v72, 0x43800000, v37
	v_mul_f32_e32 v85, 0x43800000, v41
	v_med3_f32 v72, v72, s17, v79
	v_med3_f32 v85, v85, s17, v79
	v_mov_b32_e32 v87, 0
	v_cvt_pk_fp8_f32 v87, v72, v85
	v_mul_f32_e32 v86, 0x43800000, v45
	v_mul_f32_e32 v72, 0x43800000, v49
	v_med3_f32 v85, v86, s17, v79
	v_med3_f32 v72, v72, s17, v79
	v_cvt_pk_fp8_f32 v87, v85, v72 op_sel:[0,0,1]
	s_add_i32 s22, s15, s19
	v_add3_u32 v72, s21, v75, v83
	s_cmpk_gt_i32 s22, 0x15ff
	ds_write_b32 v72, v87
	s_cbranch_scc1 .LBB0_292
	s_ashr_i32 s23, s22, 31
	s_lshr_b32 s23, s23, 23
	s_add_i32 s23, s22, s23
	s_ashr_i32 s24, s23, 9
	s_and_b32 s23, s23, 0xfe00
	s_ashr_i32 s25, s24, 31
	s_sub_i32 s26, s22, s23
	s_lshl_b64 s[22:23], s[24:25], 24
	v_lshl_add_u64 v[34:35], v[66:67], 0, s[22:23]
	s_sext_i32_i16 s22, s26
	s_bfe_u32 s22, s22, 0x4001b
	s_add_i32 s22, s26, s22
	s_sext_i32_i16 s23, s22
	s_and_b32 s22, s22, 0xfff0
	s_sub_i32 s22, s26, s22
	s_sext_i32_i16 s24, s22
	s_lshl_b32 s22, s23, 2
	s_andn2_b32 s22, s22, 63
	v_lshl_add_u32 v42, s24, 7, v78
	s_ashr_i32 s23, s22, 31
	v_lshl_add_u64 v[34:35], s[22:23], 2, v[34:35]
	v_lshlrev_b32_e32 v72, 2, v68
	v_ashrrev_i32_e32 v43, 31, v42
	v_lshl_add_u64 v[44:45], v[34:35], 0, v[72:73]
	v_lshlrev_b64 v[34:35], 13, v[42:43]
	v_lshl_add_u64 v[46:47], v[44:45], 0, v[34:35]
	v_or_b32_e32 v34, 1, v42
	v_ashrrev_i32_e32 v35, 31, v34
	v_lshlrev_b64 v[34:35], 13, v[34:35]
	v_lshl_add_u64 v[48:49], v[44:45], 0, v[34:35]
	flat_load_dwordx4 v[34:37], v[46:47] nt
	flat_load_dwordx4 v[38:41], v[48:49] nt
	v_or_b32_e32 v46, 2, v42
	v_ashrrev_i32_e32 v47, 31, v46
	v_or_b32_e32 v42, 3, v42
	v_lshlrev_b64 v[46:47], 13, v[46:47]
	v_ashrrev_i32_e32 v43, 31, v42
	v_lshl_add_u64 v[86:87], v[44:45], 0, v[46:47]
	v_lshlrev_b64 v[42:43], 13, v[42:43]
	v_lshl_add_u64 v[88:89], v[44:45], 0, v[42:43]
	flat_load_dwordx4 v[42:45], v[86:87] nt
	flat_load_dwordx4 v[46:49], v[88:89] nt

; #define LAS __attribute__((address_space(3)))
; #define TB_LOAD(R_, t_) do { const int _t = (t_); if (_t < tot) { const int _b = _t / per, _r = _t % per; ttb_load(R_, src + (size_t)_b * K_ * N_, N_, (_r % kt) * 128, (_r / kt) * 64, C.tid); } } while (0)
; __device__ __forceinline__ void ttb_load(TReg& R, const float* src, int ld, int k0, int n0, int tid) {
;     const int kr = tid >> 4, nq = tid & 15;
; #pragma unroll
;     for (int rep = 0; rep < 4; ++rep) R.v[rep] = __builtin_nontemporal_load((const f32x4*)(src + (size_t)(k0 + 4 * kr + rep) * ld + n0 + 4 * nq)); }
; __device__ __forceinline__ void ttb_put(const TReg& R, LAS unsigned* tile, int tid) {
;     const int kr = tid >> 4, nq = tid & 15;
; #pragma unroll
;     for (int c = 0; c < 4; ++c) { const int n = 4 * nq + c;
;         tile[n * 32 + (kr ^ (n & 31))] = pk4_fp8(R.v[0][c] * W_FP8_SCALE, R.v[1][c] * W_FP8_SCALE, R.v[2][c] * W_FP8_SCALE, R.v[3][c] * W_FP8_SCALE); } }
; __device__ __forceinline__ void ttb_finish(LAS const unsigned* tile, unsigned char* dst, int ldd, int k0, int n0, int map, int tid) {
;     const int n = tid >> 3, kq = tid & 7, m = n & 31, ns = n0 + n; int r = ns;
;     if (map == 2) { const int j = ns >> 1, par = ns & 1; r = 256 * (j >> 7) + 128 * par + (j & 127); }
;     const u32x4 g = *(LAS const u32x4*)(tile + n * 32 + 4 * (kq ^ (m >> 2)));
;     const unsigned a0 = (m & 1) ? g.y : g.x, a1 = (m & 1) ? g.x : g.y, a2 = (m & 1) ? g.w : g.z, a3 = (m & 1) ? g.z : g.w;
;     u32x4 w; w.x = (m & 2) ? a2 : a0; w.y = (m & 2) ? a3 : a1; w.z = (m & 2) ? a0 : a2; w.w = (m & 2) ? a1 : a3;
;     __builtin_nontemporal_store(w, (u32x4*)(dst + (size_t)r * ldd + k0 + 16 * kq));
; }
; template <int K_, int N_, int MAP_> __device__ __forceinline__ void tjob_b(const Ctx& C, int bid, int G, const float* src, unsigned char* dstb, int nbatch) {
;     constexpr int kt = K_ / 128, ntile = N_ / 64, per = kt * ntile; const int tot = per * nbatch;
;     TReg R0, R1, R2, R3; int kbuf = 0;
;     ...
;     TB_LOAD(R0, bid); TB_LOAD(R1, bid + G); TB_LOAD(R2, bid + 2 * G); TB_LOAD(R3, bid + 3 * G);
;     for (int t = bid; t < tot; t += 4 * G) { TB_STEP(R0, t); TB_STEP(R1, t + G); TB_STEP(R2, t + 2 * G); TB_STEP(R3, t + 3 * G); }
.LBB0_293:
	s_add_i32 s20, s11, s19
	s_cmpk_gt_i32 s20, 0x15ff
	s_cbranch_scc1 .LBB0_282
	v_mul_f32_e32 v72, 0x43800000, v50
	v_mul_f32_e32 v85, 0x43800000, v54
	v_med3_f32 v72, v72, s17, v79
	v_med3_f32 v85, v85, s17, v79
	v_mov_b32_e32 v87, 0
	v_cvt_pk_fp8_f32 v87, v72, v85
	v_mul_f32_e32 v86, 0x43800000, v58
	v_mul_f32_e32 v72, 0x43800000, v62
	v_med3_f32 v85, v86, s17, v79
	v_med3_f32 v72, v72, s17, v79
	v_cvt_pk_fp8_f32 v87, v85, v72 op_sel:[0,0,1]
	s_lshl_b32 s21, s13, 13
	s_add_i32 s21, s21, 0
	v_add3_u32 v72, s21, v1, v80
	ds_write_b32 v72, v87
	v_mul_f32_e32 v72, 0x43800000, v51
	v_mul_f32_e32 v85, 0x43800000, v55
	v_med3_f32 v72, v72, s17, v79
	v_med3_f32 v85, v85, s17, v79
	v_mov_b32_e32 v87, 0
	v_cvt_pk_fp8_f32 v87, v72, v85
	v_mul_f32_e32 v86, 0x43800000, v59
	v_mul_f32_e32 v72, 0x43800000, v63
	v_med3_f32 v85, v86, s17, v79
	v_med3_f32 v72, v72, s17, v79
	v_cvt_pk_fp8_f32 v87, v85, v72 op_sel:[0,0,1]
	v_mul_f32_e32 v72, 0x43800000, v52
	v_mul_f32_e32 v85, 0x43800000, v56
	v_med3_f32 v72, v72, s17, v79
	v_med3_f32 v85, v85, s17, v79
	v_mov_b32_e32 v88, 0
	v_cvt_pk_fp8_f32 v88, v72, v85
	v_mul_f32_e32 v86, 0x43800000, v60
	v_mul_f32_e32 v72, 0x43800000, v64
	v_med3_f32 v85, v86, s17, v79
	v_med3_f32 v72, v72, s17, v79
	v_cvt_pk_fp8_f32 v88, v85, v72 op_sel:[0,0,1]
	v_add3_u32 v72, s21, v69, v81
	ds_write_b32 v72, v87
	v_add3_u32 v72, s21, v74, v82
	ds_write_b32 v72, v88
	v_mul_f32_e32 v72, 0x43800000, v53
	v_mul_f32_e32 v85, 0x43800000, v57
	v_med3_f32 v72, v72, s17, v79
	v_med3_f32 v85, v85, s17, v79
	v_mov_b32_e32 v87, 0
	v_cvt_pk_fp8_f32 v87, v72, v85
	v_mul_f32_e32 v86, 0x43800000, v61
	v_mul_f32_e32 v72, 0x43800000, v65
	v_med3_f32 v85, v86, s17, v79
	v_med3_f32 v72, v72, s17, v79
	v_cvt_pk_fp8_f32 v87, v85, v72 op_sel:[0,0,1]
	s_add_i32 s19, s14, s19
	v_add3_u32 v72, s21, v75, v83
	s_cmpk_gt_i32 s19, 0x15ff
	ds_write_b32 v72, v87
	s_cbranch_scc1 .LBB0_281
	s_ashr_i32 s22, s19, 31
	s_lshr_b32 s22, s22, 23
	s_add_i32 s23, s19, s22
	s_ashr_i32 s22, s23, 9
	s_and_b32 s23, s23, 0xfe00
	s_sub_i32 s19, s19, s23
	s_ashr_i32 s23, s22, 31
	s_lshl_b64 s[22:23], s[22:23], 24
	v_lshl_add_u64 v[50:51], v[66:67], 0, s[22:23]
	s_sext_i32_i16 s22, s19
	s_bfe_u32 s22, s22, 0x4001b
	s_add_i32 s22, s19, s22
	s_sext_i32_i16 s23, s22
	s_and_b32 s22, s22, 0xfff0
	s_sub_i32 s19, s19, s22
	s_lshl_b32 s22, s23, 2
	s_sext_i32_i16 s19, s19
	s_andn2_b32 s22, s22, 63
	v_lshl_add_u32 v58, s19, 7, v78
	s_ashr_i32 s23, s22, 31
	v_lshl_add_u64 v[50:51], s[22:23], 2, v[50:51]
	v_lshlrev_b32_e32 v72, 2, v68
	v_ashrrev_i32_e32 v59, 31, v58
	v_lshl_add_u64 v[60:61], v[50:51], 0, v[72:73]
	v_lshlrev_b64 v[50:51], 13, v[58:59]
	v_lshl_add_u64 v[62:63], v[60:61], 0, v[50:51]
	v_or_b32_e32 v50, 1, v58
	v_ashrrev_i32_e32 v51, 31, v50
	v_lshlrev_b64 v[50:51], 13, v[50:51]
	v_lshl_add_u64 v[64:65], v[60:61], 0, v[50:51]
	flat_load_dwordx4 v[50:53], v[62:63] nt
	flat_load_dwordx4 v[54:57], v[64:65] nt
	v_or_b32_e32 v62, 2, v58
	v_ashrrev_i32_e32 v63, 31, v62
	v_or_b32_e32 v58, 3, v58
	v_lshlrev_b64 v[62:63], 13, v[62:63]
	v_ashrrev_i32_e32 v59, 31, v58
	v_lshl_add_u64 v[86:87], v[60:61], 0, v[62:63]
	v_lshlrev_b64 v[58:59], 13, v[58:59]
	v_lshl_add_u64 v[88:89], v[60:61], 0, v[58:59]
	flat_load_dwordx4 v[58:61], v[86:87] nt
	flat_load_dwordx4 v[62:65], v[88:89] nt
	s_branch .LBB0_281

; #define IN(k) (fresh_tid(C), lo <= (k) && (k) < hi)
; #define SEAM(k) do { if (IN(k) && IN((k) + 1)) xcd_barrier(bar); } while (0)
;     __host__ __device__ bool map(int i, int& pm, int& pn) const {
;         const int L = i * G + c; if (L >= nwg || c < 0) return false;
;         int wgid = L; { const int q = nwg / NXCD, r = nwg % NXCD, xcd = wgid % NXCD, off = wgid / NXCD; wgid = (xcd < r ? xcd * (q + 1) : r * (q + 1) + (xcd - r) * q) + off; }
;         const int nig = WGM * nN, gid = wgid / nig, fm = gid * WGM, gsz = (nM - fm) < WGM ? (nM - fm) : WGM;
;         pm = fm + ((wgid % nig) % gsz); pn = (wgid % nig) / gsz; return true;
;     }
; __global__ void __launch_bounds__(512, 2) mk_fwd(Args args) {
;     ...
;     if (IN(6)) for (int rep_ = ((MK_REPEAT >> 6) & 1) ? 0 : 1; rep_ < 2; ++rep_) { pg8::Gemm g{WSP(bf16_t, WS_MIX), WSP(bf16_t, WS_WOUT), T_, D_, MIXP / 2}; pg8::StaticOrder S; S.init(T_, D_, C.G, C.bid); pg8::EpiResF32 E{C.ka, C.ws, D_, rep_ ? WS_ROWSS : WS_PROJ, 1.0f / (MIX_SCALE * W_FP8_SCALE)};
;         pg8::gemm_phase<pg8::EpiResF32, pg8::StaticOrder, false, 2>(C.lds, g, S, E); if (!rep_) xcd_barrier(bar); } SEAM(6);
.LBB0_803:
	s_cmp_lt_i32 s82, 7
	s_cselect_b64 s[0:1], -1, 0
	s_cmp_gt_i32 s83, 6
	v_mov_b32_e32 v1, v0
	s_cselect_b64 s[2:3], -1, 0
	s_and_b64 s[0:1], s[0:1], s[2:3]
	v_cndmask_b32_e64 v1, 0, 1, s[0:1]
	v_cmp_ne_u32_e64 s[4:5], 1, v1
	s_andn2_b64 vcc, exec, s[0:1]
	s_mov_b64 s[54:55], s[80:81]
	s_cbranch_vccnz .LBB0_840
	v_readlane_b32 s0, v254, 0
	s_nop 3
	s_bfe_u32 s0, s0, 0x20003
	s_lshl_b32 s0, s0, 1
	s_cmp_eq_u32 s0, 0
	s_cbranch_scc1 .Lp6_nosleep
.Lp6_sleep:
	s_sleep 127
	s_sub_u32 s0, s0, 1
	s_cmp_lg_u32 s0, 0
	s_cbranch_scc1 .Lp6_sleep
.Lp6_nosleep:
	v_readlane_b32 s0, v254, 0
	v_readlane_b32 s1, v254, 1
	s_mov_b32 s2, s0
	s_cmpk_lt_u32 s0, 0x400
	v_mov_b32_e32 v2, v0
	s_cselect_b64 s[0:1], -1, 0
	s_cmpk_gt_u32 s2, 0x3ff
	s_nop 0
	v_readfirstlane_b32 s17, v2
	s_cbranch_scc1 .LBB0_806
	v_readlane_b32 s2, v254, 0
	v_readlane_b32 s3, v254, 1
	s_mov_b32 s6, s2
	s_lshl_b32 s2, s2, 7
	s_lshr_b32 s3, s6, 3
	s_or_b32 s2, s2, s3
	s_lshr_b32 s2, s2, 3
	s_and_b32 s2, s2, 0x78
	s_bfe_u32 s3, s6, 0x30003
	s_or_b32 s46, s2, s3
	s_bfe_u32 s45, s6, 0x30006
